# split grid barrier 9: attention preamble (unit list + bitonic sort) runs between arrive and wait; first-tile table published by scan blocks through a ready counter
# baseline (speedup 1.0000x reference)
.LBB0_1371:
	s_or_b64 exec, exec, s[4:5]
	s_waitcnt lgkmcnt(0)
	s_barrier
	s_and_saveexec_b64 s[4:5], s[6:7]
	s_cbranch_execz .LBB0_1373
	v_lshl_add_u32 v1, v0, 2, 0
	ds_read_b32 v1, v1 offset:128
	v_lshl_or_b32 v2, s18, 5, v0
	v_readlane_b32 s36, v253, 46
	v_ashrrev_i32_e32 v3, 31, v2
	v_readlane_b32 s50, v253, 60
	v_readlane_b32 s51, v253, 61
	s_waitcnt lgkmcnt(0)
	v_min_i32_e32 v1, v1, v252
	v_and_b32_e32 v1, -2, v1
	v_lshl_add_u64 v[2:3], v[2:3], 2, s[50:51]
	v_add_co_u32_e32 v2, vcc, 0x1582000, v2
	v_readlane_b32 s37, v253, 47
	s_nop 0
	v_addc_co_u32_e32 v3, vcc, 0, v3, vcc
	v_readlane_b32 s38, v253, 48
	v_readlane_b32 s39, v253, 49
	v_readlane_b32 s40, v253, 50
	v_readlane_b32 s41, v253, 51
	v_readlane_b32 s42, v253, 52
	v_readlane_b32 s43, v253, 53
	v_readlane_b32 s44, v253, 54
	v_readlane_b32 s45, v253, 55
	v_readlane_b32 s46, v253, 56
	v_readlane_b32 s47, v253, 57
	v_readlane_b32 s48, v253, 58
	v_readlane_b32 s49, v253, 59
	global_store_dword v[2:3], v1, off sc1
	s_waitcnt vmcnt(0)
	v_mov_b32_e32 v2, 0
	v_mov_b32_e32 v3, 1
	global_atomic_add v2, v3, s[100:101] offset:128

.LBB0_1606:
	s_cmp_gt_i32 s81, 10
	s_cselect_b64 s[0:1], -1, 0
	s_and_b64 s[4:5], s[12:13], s[0:1]
	s_andn2_b64 vcc, exec, s[4:5]
	s_waitcnt vmcnt(0)
	v_and_b32_e32 v82, 63, v0
	s_cbranch_vccnz .LBB0_1660
	s_waitcnt vmcnt(0)
	s_waitcnt lgkmcnt(0)
	s_barrier
	s_and_saveexec_b64 s[4:5], s[78:79]
	s_cbranch_execz .LBB0_1659
	v_mov_b32_e32 v1, 0x22160
	s_waitcnt vmcnt(0) lgkmcnt(0)
	ds_read_b32 v2, v1
	v_mov_b32_e32 v3, 1
	v_mov_b32_e32 v4, s99
	v_and_b32_e32 v5, 0xffff, v4
	v_lshrrev_b32_e32 v6, 16, v4
	global_atomic_add v7, v5, v3, s[100:101] sc0
	buffer_inv sc1
	v_mov_b32_e32 v12, 0
	global_load_dword v11, v12, s[100:101] offset:128 sc1
	v_lshrrev_b32_e32 v8, 8, v5
	v_sub_u32_e32 v8, s98, v8
	v_add_u32_e32 v8, 7, v8
	v_lshrrev_b32_e32 v8, 3, v8
	v_mov_b32_e32 v9, s98
	v_min_u32_e32 v9, 8, v9
	v_mov_b32_e32 v10, 0
	s_waitcnt lgkmcnt(0)
	v_add_u32_e32 v2, 1, v2
	ds_write_b32 v1, v2
	v_mul_lo_u32 v8, v8, v2
	v_mul_lo_u32 v9, v9, v2
	s_waitcnt vmcnt(0)
	v_add_u32_e32 v7, 1, v7
	v_cmp_eq_u32_e32 vcc, v7, v8
	s_cbranch_vccz .Lgb_chk_9
	v_mov_b32_e32 v4, 0
	global_atomic_add v4, v3, s[100:101] offset:2048
	global_atomic_add v4, v3, s[100:101] offset:2304
	global_atomic_add v4, v3, s[100:101] offset:2560
	global_atomic_add v4, v3, s[100:101] offset:2816
	global_atomic_add v4, v3, s[100:101] offset:3072
	global_atomic_add v4, v3, s[100:101] offset:3328
	global_atomic_add v4, v3, s[100:101] offset:3584
	global_atomic_add v4, v3, s[100:101] offset:3840
.Lgb_chk_9:
	v_mov_b32_e32 v6, 0x80
	v_mov_b32_e32 v9, 0x400
	v_cmp_ge_u32_e32 vcc, v11, v9
	s_cbranch_vccnz .Lgb_done_9

.LBB0_1687:
	s_or_b64 exec, exec, s[6:7]
	v_add_u32_e32 v1, s30, v2
	ds_write_b32 v1, v3 offset:4
	v_add_u32_e32 v1, s30, v250
	s_waitcnt lgkmcnt(0)
	s_barrier
	ds_read_b128 v[8:11], v1
	v_cmp_eq_u32_e32 vcc, 0, v192
	s_waitcnt lgkmcnt(0)
	s_barrier
	v_and_b32_e32 v17, 0x80, v0
	v_and_b32_e32 v205, 31, v0
	s_waitcnt lgkmcnt(0)
	v_max_i32_e32 v2, v8, v9
	v_min_i32_e32 v6, v10, v11
	v_min_i32_e32 v3, v8, v9
	v_max_i32_e32 v5, v10, v11
	v_max_i32_e32 v8, v2, v6
	v_min_i32_e32 v2, v2, v6
	v_cndmask_b32_e32 v6, v2, v8, vcc
	v_cndmask_b32_e32 v2, v8, v2, vcc
	v_max_i32_e32 v8, v3, v5
	v_min_i32_e32 v3, v3, v5
	v_cndmask_b32_e32 v5, v3, v8, vcc
	v_cndmask_b32_e32 v3, v8, v3, vcc
	v_max_i32_e32 v8, v6, v5
	v_min_i32_e32 v5, v6, v5
	v_cndmask_b32_e32 v6, v5, v8, vcc
	v_cndmask_b32_e32 v5, v8, v5, vcc
	v_max_i32_e32 v9, v2, v3
	v_min_i32_e32 v3, v2, v3
	v_xor_b32_e32 v2, 1, v7
	v_add_u32_e32 v8, 64, v4
	v_cmp_lt_i32_e64 s[6:7], v2, v8
	v_cndmask_b32_e32 v10, v3, v9, vcc
	v_cndmask_b32_e32 v3, v9, v3, vcc
	v_cndmask_b32_e64 v2, v7, v2, s[6:7]
	v_lshlrev_b32_e32 v2, 2, v2
	ds_bpermute_b32 v4, v2, v6
	ds_bpermute_b32 v12, v2, v5
	v_and_b32_e32 v9, 2, v0
	v_cmp_ne_u32_e64 s[6:7], 0, v9
	s_xor_b64 s[6:7], vcc, s[6:7]
	s_waitcnt lgkmcnt(1)
	v_max_i32_e32 v11, v6, v4
	v_min_i32_e32 v4, v6, v4
	v_cndmask_b32_e64 v4, v4, v11, s[6:7]
	ds_bpermute_b32 v6, v2, v10
	s_waitcnt lgkmcnt(1)
	v_max_i32_e32 v11, v5, v12
	v_min_i32_e32 v5, v5, v12
	ds_bpermute_b32 v12, v2, v3
	v_cndmask_b32_e64 v5, v5, v11, s[6:7]
	s_waitcnt lgkmcnt(1)
	v_max_i32_e32 v11, v10, v6
	v_min_i32_e32 v6, v10, v6
	v_cndmask_b32_e64 v6, v6, v11, s[6:7]
	s_waitcnt lgkmcnt(0)
	v_max_i32_e32 v10, v3, v12
	v_min_i32_e32 v3, v3, v12
	v_cndmask_b32_e64 v3, v3, v10, s[6:7]
	v_max_i32_e32 v10, v4, v6
	v_min_i32_e32 v4, v4, v6
	v_cmp_eq_u32_e64 s[6:7], 0, v9
	v_max_i32_e32 v9, v5, v3
	v_min_i32_e32 v3, v5, v3
	v_cndmask_b32_e64 v6, v4, v10, s[6:7]
	v_cndmask_b32_e64 v5, v3, v9, s[6:7]
	v_cndmask_b32_e64 v4, v10, v4, s[6:7]
	v_cndmask_b32_e64 v3, v9, v3, s[6:7]
	v_max_i32_e32 v9, v6, v5
	v_min_i32_e32 v5, v6, v5
	v_cndmask_b32_e64 v6, v5, v9, s[6:7]
	v_cndmask_b32_e64 v5, v9, v5, s[6:7]
	v_max_i32_e32 v9, v4, v3
	v_min_i32_e32 v4, v4, v3
	v_xor_b32_e32 v3, 2, v7
	v_cmp_lt_i32_e64 s[8:9], v3, v8
	v_cndmask_b32_e64 v11, v4, v9, s[6:7]
	v_cndmask_b32_e64 v4, v9, v4, s[6:7]
	v_cndmask_b32_e64 v3, v7, v3, s[8:9]
	v_lshlrev_b32_e32 v3, 2, v3
	ds_bpermute_b32 v10, v3, v6
	ds_bpermute_b32 v13, v3, v5
	v_and_b32_e32 v9, 4, v0
	v_cmp_ne_u32_e64 s[8:9], 0, v9
	s_xor_b64 s[10:11], s[6:7], s[8:9]
	s_waitcnt lgkmcnt(1)
	v_max_i32_e32 v12, v6, v10
	v_min_i32_e32 v6, v6, v10
	v_cndmask_b32_e64 v6, v6, v12, s[10:11]
	ds_bpermute_b32 v10, v3, v11
	s_waitcnt lgkmcnt(1)
	v_max_i32_e32 v12, v5, v13
	v_min_i32_e32 v5, v5, v13
	v_cndmask_b32_e64 v5, v5, v12, s[10:11]
	ds_bpermute_b32 v12, v3, v4
	s_waitcnt lgkmcnt(1)
	v_max_i32_e32 v13, v11, v10
	v_min_i32_e32 v10, v11, v10
	ds_bpermute_b32 v11, v2, v6
	v_cndmask_b32_e64 v10, v10, v13, s[10:11]
	s_waitcnt lgkmcnt(1)
	v_max_i32_e32 v13, v4, v12
	v_min_i32_e32 v4, v4, v12
	v_cndmask_b32_e64 v4, v4, v13, s[10:11]
	ds_bpermute_b32 v13, v2, v5
	s_waitcnt lgkmcnt(1)
	v_max_i32_e32 v12, v6, v11
	v_min_i32_e32 v6, v6, v11
	s_xor_b64 s[8:9], vcc, s[8:9]
	v_cndmask_b32_e64 v6, v6, v12, s[8:9]
	ds_bpermute_b32 v11, v2, v10
	s_waitcnt lgkmcnt(1)
	v_max_i32_e32 v12, v5, v13
	v_min_i32_e32 v5, v5, v13
	ds_bpermute_b32 v13, v2, v4
	v_cndmask_b32_e64 v5, v5, v12, s[8:9]
	s_waitcnt lgkmcnt(1)
	v_max_i32_e32 v12, v10, v11
	v_min_i32_e32 v10, v10, v11
	v_cndmask_b32_e64 v10, v10, v12, s[8:9]
	s_waitcnt lgkmcnt(0)
	v_max_i32_e32 v11, v4, v13
	v_min_i32_e32 v4, v4, v13
	v_cndmask_b32_e64 v4, v4, v11, s[8:9]
	v_max_i32_e32 v11, v6, v10
	v_min_i32_e32 v6, v6, v10
	v_cmp_eq_u32_e64 s[8:9], 0, v9
	v_max_i32_e32 v10, v5, v4
	v_min_i32_e32 v4, v5, v4
	v_cndmask_b32_e64 v9, v6, v11, s[8:9]
	v_cndmask_b32_e64 v5, v4, v10, s[8:9]
	v_cndmask_b32_e64 v6, v11, v6, s[8:9]
	v_cndmask_b32_e64 v4, v10, v4, s[8:9]
	v_max_i32_e32 v10, v9, v5
	v_min_i32_e32 v5, v9, v5
	v_cndmask_b32_e64 v9, v5, v10, s[8:9]
	v_cndmask_b32_e64 v5, v10, v5, s[8:9]
	v_max_i32_e32 v10, v6, v4
	v_min_i32_e32 v6, v6, v4
	v_xor_b32_e32 v4, 4, v7
	v_cmp_lt_i32_e64 s[10:11], v4, v8
	v_cndmask_b32_e64 v12, v6, v10, s[8:9]
	v_cndmask_b32_e64 v6, v10, v6, s[8:9]
	v_cndmask_b32_e64 v4, v7, v4, s[10:11]
	v_lshlrev_b32_e32 v4, 2, v4
	ds_bpermute_b32 v11, v4, v9
	ds_bpermute_b32 v14, v4, v5
	v_and_b32_e32 v10, 8, v0
	v_cmp_ne_u32_e64 s[10:11], 0, v10
	s_xor_b64 s[12:13], s[8:9], s[10:11]
	s_waitcnt lgkmcnt(1)
	v_max_i32_e32 v13, v9, v11
	v_min_i32_e32 v9, v9, v11
	v_cndmask_b32_e64 v9, v9, v13, s[12:13]
	ds_bpermute_b32 v11, v4, v12
	s_waitcnt lgkmcnt(1)
	v_max_i32_e32 v13, v5, v14
	v_min_i32_e32 v5, v5, v14
	v_cndmask_b32_e64 v5, v5, v13, s[12:13]
	ds_bpermute_b32 v13, v4, v6
	s_waitcnt lgkmcnt(1)
	v_max_i32_e32 v14, v12, v11
	v_min_i32_e32 v11, v12, v11
	ds_bpermute_b32 v12, v3, v9
	v_cndmask_b32_e64 v11, v11, v14, s[12:13]
	s_waitcnt lgkmcnt(1)
	v_max_i32_e32 v14, v6, v13
	v_min_i32_e32 v6, v6, v13
	v_cndmask_b32_e64 v6, v6, v14, s[12:13]
	ds_bpermute_b32 v14, v3, v5
	s_waitcnt lgkmcnt(1)
	v_max_i32_e32 v13, v9, v12
	v_min_i32_e32 v9, v9, v12
	s_xor_b64 s[12:13], s[6:7], s[10:11]
	v_cndmask_b32_e64 v9, v9, v13, s[12:13]
	ds_bpermute_b32 v12, v3, v11
	s_waitcnt lgkmcnt(1)
	v_max_i32_e32 v13, v5, v14
	v_min_i32_e32 v5, v5, v14
	v_cndmask_b32_e64 v5, v5, v13, s[12:13]
	ds_bpermute_b32 v13, v3, v6
	s_waitcnt lgkmcnt(1)
	v_max_i32_e32 v14, v11, v12
	v_min_i32_e32 v11, v11, v12
	ds_bpermute_b32 v12, v2, v9
	v_cndmask_b32_e64 v11, v11, v14, s[12:13]
	s_waitcnt lgkmcnt(1)
	v_max_i32_e32 v14, v6, v13
	v_min_i32_e32 v6, v6, v13
	v_cndmask_b32_e64 v6, v6, v14, s[12:13]
	ds_bpermute_b32 v14, v2, v5
	s_waitcnt lgkmcnt(1)
	v_max_i32_e32 v13, v9, v12
	v_min_i32_e32 v9, v9, v12
	s_xor_b64 s[10:11], vcc, s[10:11]
	v_cndmask_b32_e64 v9, v9, v13, s[10:11]
	ds_bpermute_b32 v12, v2, v11
	s_waitcnt lgkmcnt(1)
	v_max_i32_e32 v13, v5, v14
	v_min_i32_e32 v5, v5, v14
	ds_bpermute_b32 v14, v2, v6
	v_cndmask_b32_e64 v5, v5, v13, s[10:11]
	s_waitcnt lgkmcnt(1)
	v_max_i32_e32 v13, v11, v12
	v_min_i32_e32 v11, v11, v12
	v_cndmask_b32_e64 v11, v11, v13, s[10:11]
	s_waitcnt lgkmcnt(0)
	v_max_i32_e32 v12, v6, v14
	v_min_i32_e32 v6, v6, v14
	v_cndmask_b32_e64 v6, v6, v12, s[10:11]
	v_max_i32_e32 v12, v9, v11
	v_min_i32_e32 v9, v9, v11
	v_cmp_eq_u32_e64 s[10:11], 0, v10
	v_max_i32_e32 v11, v5, v6
	v_min_i32_e32 v5, v5, v6
	v_cndmask_b32_e64 v10, v9, v12, s[10:11]
	v_cndmask_b32_e64 v6, v5, v11, s[10:11]
	v_cndmask_b32_e64 v9, v12, v9, s[10:11]
	v_cndmask_b32_e64 v5, v11, v5, s[10:11]
	v_max_i32_e32 v11, v10, v6
	v_min_i32_e32 v6, v10, v6
	v_cndmask_b32_e64 v10, v6, v11, s[10:11]
	v_cndmask_b32_e64 v6, v11, v6, s[10:11]
	v_max_i32_e32 v11, v9, v5
	v_min_i32_e32 v9, v9, v5
	v_xor_b32_e32 v5, 8, v7
	v_cmp_lt_i32_e64 s[12:13], v5, v8
	v_cndmask_b32_e64 v13, v9, v11, s[10:11]
	v_cndmask_b32_e64 v9, v11, v9, s[10:11]
	v_cndmask_b32_e64 v5, v7, v5, s[12:13]
	v_lshlrev_b32_e32 v5, 2, v5
	ds_bpermute_b32 v12, v5, v10
	ds_bpermute_b32 v15, v5, v6
	v_and_b32_e32 v11, 16, v0
	v_cmp_ne_u32_e64 s[12:13], 0, v11
	s_xor_b64 s[14:15], s[10:11], s[12:13]
	s_waitcnt lgkmcnt(1)
	v_max_i32_e32 v14, v10, v12
	v_min_i32_e32 v10, v10, v12
	v_cndmask_b32_e64 v10, v10, v14, s[14:15]
	ds_bpermute_b32 v12, v5, v13
	s_waitcnt lgkmcnt(1)
	v_max_i32_e32 v14, v6, v15
	v_min_i32_e32 v6, v6, v15
	v_cndmask_b32_e64 v6, v6, v14, s[14:15]
	ds_bpermute_b32 v14, v5, v9
	s_waitcnt lgkmcnt(1)
	v_max_i32_e32 v15, v13, v12
	v_min_i32_e32 v12, v13, v12
	ds_bpermute_b32 v13, v4, v10
	v_cndmask_b32_e64 v12, v12, v15, s[14:15]
	s_waitcnt lgkmcnt(1)
	v_max_i32_e32 v15, v9, v14
	v_min_i32_e32 v9, v9, v14
	v_cndmask_b32_e64 v9, v9, v15, s[14:15]
	ds_bpermute_b32 v15, v4, v6
	s_waitcnt lgkmcnt(1)
	v_max_i32_e32 v14, v10, v13
	v_min_i32_e32 v10, v10, v13
	s_xor_b64 s[14:15], s[8:9], s[12:13]
	v_cndmask_b32_e64 v10, v10, v14, s[14:15]
	ds_bpermute_b32 v13, v4, v12
	s_waitcnt lgkmcnt(1)
	v_max_i32_e32 v14, v6, v15
	v_min_i32_e32 v6, v6, v15
	v_cndmask_b32_e64 v6, v6, v14, s[14:15]
	ds_bpermute_b32 v14, v4, v9
	s_waitcnt lgkmcnt(1)
	v_max_i32_e32 v15, v12, v13
	v_min_i32_e32 v12, v12, v13
	ds_bpermute_b32 v13, v3, v10
	v_cndmask_b32_e64 v12, v12, v15, s[14:15]
	s_waitcnt lgkmcnt(1)
	v_max_i32_e32 v15, v9, v14
	v_min_i32_e32 v9, v9, v14
	v_cndmask_b32_e64 v9, v9, v15, s[14:15]
	ds_bpermute_b32 v15, v3, v6
	s_waitcnt lgkmcnt(1)
	v_max_i32_e32 v14, v10, v13
	v_min_i32_e32 v10, v10, v13
	s_xor_b64 s[14:15], s[6:7], s[12:13]
	v_cndmask_b32_e64 v10, v10, v14, s[14:15]
	ds_bpermute_b32 v13, v3, v12
	s_waitcnt lgkmcnt(1)
	v_max_i32_e32 v14, v6, v15
	v_min_i32_e32 v6, v6, v15
	v_cndmask_b32_e64 v6, v6, v14, s[14:15]
	ds_bpermute_b32 v14, v3, v9
	s_waitcnt lgkmcnt(1)
	v_max_i32_e32 v15, v12, v13
	v_min_i32_e32 v12, v12, v13
	ds_bpermute_b32 v13, v2, v10
	v_cndmask_b32_e64 v12, v12, v15, s[14:15]
	s_waitcnt lgkmcnt(1)
	v_max_i32_e32 v15, v9, v14
	v_min_i32_e32 v9, v9, v14
	v_cndmask_b32_e64 v9, v9, v15, s[14:15]
	ds_bpermute_b32 v15, v2, v6
	s_waitcnt lgkmcnt(1)
	v_max_i32_e32 v14, v10, v13
	v_min_i32_e32 v10, v10, v13
	s_xor_b64 s[12:13], vcc, s[12:13]
	v_cndmask_b32_e64 v10, v10, v14, s[12:13]
	ds_bpermute_b32 v13, v2, v12
	s_waitcnt lgkmcnt(1)
	v_max_i32_e32 v14, v6, v15
	v_min_i32_e32 v6, v6, v15
	ds_bpermute_b32 v15, v2, v9
	v_cndmask_b32_e64 v6, v6, v14, s[12:13]
	s_waitcnt lgkmcnt(1)
	v_max_i32_e32 v14, v12, v13
	v_min_i32_e32 v12, v12, v13
	v_cndmask_b32_e64 v12, v12, v14, s[12:13]
	s_waitcnt lgkmcnt(0)
	v_max_i32_e32 v13, v9, v15
	v_min_i32_e32 v9, v9, v15
	v_cndmask_b32_e64 v9, v9, v13, s[12:13]
	v_max_i32_e32 v13, v10, v12
	v_min_i32_e32 v10, v10, v12
	v_cmp_eq_u32_e64 s[12:13], 0, v11
	v_max_i32_e32 v12, v6, v9
	v_min_i32_e32 v6, v6, v9
	v_cndmask_b32_e64 v11, v10, v13, s[12:13]
	v_cndmask_b32_e64 v9, v6, v12, s[12:13]
	v_cndmask_b32_e64 v10, v13, v10, s[12:13]
	v_cndmask_b32_e64 v6, v12, v6, s[12:13]
	v_max_i32_e32 v12, v11, v9
	v_min_i32_e32 v9, v11, v9
	v_cndmask_b32_e64 v11, v9, v12, s[12:13]
	v_cndmask_b32_e64 v9, v12, v9, s[12:13]
	v_max_i32_e32 v12, v10, v6
	v_min_i32_e32 v10, v10, v6
	v_xor_b32_e32 v6, 16, v7
	v_cmp_lt_i32_e64 s[14:15], v6, v8
	v_cndmask_b32_e64 v14, v10, v12, s[12:13]
	v_cndmask_b32_e64 v10, v12, v10, s[12:13]
	v_cndmask_b32_e64 v6, v7, v6, s[14:15]
	v_lshlrev_b32_e32 v6, 2, v6
	ds_bpermute_b32 v13, v6, v11
	ds_bpermute_b32 v16, v6, v9
	v_and_b32_e32 v12, 32, v0
	v_cmp_ne_u32_e64 s[14:15], 0, v12
	s_xor_b64 s[16:17], s[12:13], s[14:15]
	s_waitcnt lgkmcnt(1)
	v_max_i32_e32 v15, v11, v13
	v_min_i32_e32 v11, v11, v13
	v_cndmask_b32_e64 v11, v11, v15, s[16:17]
	ds_bpermute_b32 v13, v6, v14
	s_waitcnt lgkmcnt(1)
	v_max_i32_e32 v15, v9, v16
	v_min_i32_e32 v9, v9, v16
	v_cndmask_b32_e64 v9, v9, v15, s[16:17]
	ds_bpermute_b32 v15, v6, v10
	s_waitcnt lgkmcnt(1)
	v_max_i32_e32 v16, v14, v13
	v_min_i32_e32 v13, v14, v13
	ds_bpermute_b32 v14, v5, v11
	v_cndmask_b32_e64 v13, v13, v16, s[16:17]
	s_waitcnt lgkmcnt(1)
	v_max_i32_e32 v16, v10, v15
	v_min_i32_e32 v10, v10, v15
	v_cndmask_b32_e64 v10, v10, v16, s[16:17]
	ds_bpermute_b32 v16, v5, v9
	s_waitcnt lgkmcnt(1)
	v_max_i32_e32 v15, v11, v14
	v_min_i32_e32 v11, v11, v14
	s_xor_b64 s[16:17], s[10:11], s[14:15]
	v_cndmask_b32_e64 v11, v11, v15, s[16:17]
	ds_bpermute_b32 v14, v5, v13
	s_waitcnt lgkmcnt(1)
	v_max_i32_e32 v15, v9, v16
	v_min_i32_e32 v9, v9, v16
	v_cndmask_b32_e64 v9, v9, v15, s[16:17]
	ds_bpermute_b32 v15, v5, v10
	s_waitcnt lgkmcnt(1)
	v_max_i32_e32 v16, v13, v14
	v_min_i32_e32 v13, v13, v14
	ds_bpermute_b32 v14, v4, v11
	v_cndmask_b32_e64 v13, v13, v16, s[16:17]
	s_waitcnt lgkmcnt(1)
	v_max_i32_e32 v16, v10, v15
	v_min_i32_e32 v10, v10, v15
	v_cndmask_b32_e64 v10, v10, v16, s[16:17]
	ds_bpermute_b32 v16, v4, v9
	s_waitcnt lgkmcnt(1)
	v_max_i32_e32 v15, v11, v14
	v_min_i32_e32 v11, v11, v14
	s_xor_b64 s[16:17], s[8:9], s[14:15]
	v_cndmask_b32_e64 v11, v11, v15, s[16:17]
	ds_bpermute_b32 v14, v4, v13
	s_waitcnt lgkmcnt(1)
	v_max_i32_e32 v15, v9, v16
	v_min_i32_e32 v9, v9, v16
	v_cndmask_b32_e64 v9, v9, v15, s[16:17]
	ds_bpermute_b32 v15, v4, v10
	s_waitcnt lgkmcnt(1)
	v_max_i32_e32 v16, v13, v14
	v_min_i32_e32 v13, v13, v14
	ds_bpermute_b32 v14, v3, v11
	v_cndmask_b32_e64 v13, v13, v16, s[16:17]
	s_waitcnt lgkmcnt(1)
	v_max_i32_e32 v16, v10, v15
	v_min_i32_e32 v10, v10, v15
	v_cndmask_b32_e64 v10, v10, v16, s[16:17]
	ds_bpermute_b32 v16, v3, v9
	s_waitcnt lgkmcnt(1)
	v_max_i32_e32 v15, v11, v14
	v_min_i32_e32 v11, v11, v14
	s_xor_b64 s[16:17], s[6:7], s[14:15]
	v_cndmask_b32_e64 v11, v11, v15, s[16:17]
	ds_bpermute_b32 v14, v3, v13
	s_waitcnt lgkmcnt(1)
	v_max_i32_e32 v15, v9, v16
	v_min_i32_e32 v9, v9, v16
	v_cndmask_b32_e64 v9, v9, v15, s[16:17]
	ds_bpermute_b32 v15, v3, v10
	s_waitcnt lgkmcnt(1)
	v_max_i32_e32 v16, v13, v14
	v_min_i32_e32 v13, v13, v14
	ds_bpermute_b32 v14, v2, v11
	v_cndmask_b32_e64 v13, v13, v16, s[16:17]
	s_waitcnt lgkmcnt(1)
	v_max_i32_e32 v16, v10, v15
	v_min_i32_e32 v10, v10, v15
	v_cndmask_b32_e64 v10, v10, v16, s[16:17]
	ds_bpermute_b32 v16, v2, v9
	s_waitcnt lgkmcnt(1)
	v_max_i32_e32 v15, v11, v14
	v_min_i32_e32 v11, v11, v14
	s_xor_b64 s[14:15], vcc, s[14:15]
	v_cndmask_b32_e64 v11, v11, v15, s[14:15]
	ds_bpermute_b32 v14, v2, v13
	s_waitcnt lgkmcnt(1)
	v_max_i32_e32 v15, v9, v16
	v_min_i32_e32 v9, v9, v16
	ds_bpermute_b32 v16, v2, v10
	v_cndmask_b32_e64 v9, v9, v15, s[14:15]
	s_waitcnt lgkmcnt(1)
	v_max_i32_e32 v15, v13, v14
	v_min_i32_e32 v13, v13, v14
	v_cndmask_b32_e64 v13, v13, v15, s[14:15]
	s_waitcnt lgkmcnt(0)
	v_max_i32_e32 v14, v10, v16
	v_min_i32_e32 v10, v10, v16
	v_cndmask_b32_e64 v10, v10, v14, s[14:15]
	v_max_i32_e32 v14, v11, v13
	v_min_i32_e32 v11, v11, v13
	v_cmp_eq_u32_e64 s[14:15], 0, v12
	v_max_i32_e32 v13, v9, v10
	v_min_i32_e32 v9, v9, v10
	v_cndmask_b32_e64 v12, v11, v14, s[14:15]
	v_cndmask_b32_e64 v10, v9, v13, s[14:15]
	v_cndmask_b32_e64 v11, v14, v11, s[14:15]
	v_cndmask_b32_e64 v9, v13, v9, s[14:15]
	v_max_i32_e32 v13, v12, v10
	v_min_i32_e32 v10, v12, v10
	v_cndmask_b32_e64 v12, v10, v13, s[14:15]
	v_cndmask_b32_e64 v10, v13, v10, s[14:15]
	v_max_i32_e32 v13, v11, v9
	v_min_i32_e32 v9, v11, v9
	v_xor_b32_e32 v11, 32, v7
	v_cmp_lt_i32_e64 s[16:17], v11, v8
	v_mov_b32_e32 v251, v197
	s_mov_b32 s31, 0
	v_cndmask_b32_e64 v7, v7, v11, s[16:17]
	v_lshlrev_b32_e32 v7, 2, v7
	ds_bpermute_b32 v8, v7, v12
	ds_bpermute_b32 v15, v7, v10
	v_cndmask_b32_e64 v11, v9, v13, s[14:15]
	v_cndmask_b32_e64 v9, v13, v9, s[14:15]
	v_and_b32_e32 v13, 64, v0
	v_cmp_ne_u32_e64 s[16:17], 0, v13
	s_waitcnt lgkmcnt(1)
	v_max_i32_e32 v14, v12, v8
	v_min_i32_e32 v8, v12, v8
	s_xor_b64 s[18:19], s[14:15], s[16:17]
	v_cndmask_b32_e64 v8, v8, v14, s[18:19]
	ds_bpermute_b32 v12, v7, v11
	s_waitcnt lgkmcnt(1)
	v_max_i32_e32 v14, v10, v15
	v_min_i32_e32 v10, v10, v15
	v_cndmask_b32_e64 v10, v10, v14, s[18:19]
	ds_bpermute_b32 v14, v7, v9
	s_waitcnt lgkmcnt(1)
	v_max_i32_e32 v15, v11, v12
	v_min_i32_e32 v11, v11, v12
	ds_bpermute_b32 v12, v6, v8
	v_cndmask_b32_e64 v11, v11, v15, s[18:19]
	s_waitcnt lgkmcnt(1)
	v_max_i32_e32 v15, v9, v14
	v_min_i32_e32 v9, v9, v14
	v_cndmask_b32_e64 v9, v9, v15, s[18:19]
	ds_bpermute_b32 v15, v6, v10
	s_waitcnt lgkmcnt(1)
	v_max_i32_e32 v14, v8, v12
	v_min_i32_e32 v8, v8, v12
	s_xor_b64 s[18:19], s[12:13], s[16:17]
	v_cndmask_b32_e64 v8, v8, v14, s[18:19]
	ds_bpermute_b32 v12, v6, v11
	s_waitcnt lgkmcnt(1)
	v_max_i32_e32 v14, v10, v15
	v_min_i32_e32 v10, v10, v15
	v_cndmask_b32_e64 v10, v10, v14, s[18:19]
	ds_bpermute_b32 v14, v6, v9
	s_waitcnt lgkmcnt(1)
	v_max_i32_e32 v15, v11, v12
	v_min_i32_e32 v11, v11, v12
	ds_bpermute_b32 v12, v5, v8
	v_cndmask_b32_e64 v11, v11, v15, s[18:19]
	s_waitcnt lgkmcnt(1)
	v_max_i32_e32 v15, v9, v14
	v_min_i32_e32 v9, v9, v14
	v_cndmask_b32_e64 v9, v9, v15, s[18:19]
	ds_bpermute_b32 v15, v5, v10
	s_waitcnt lgkmcnt(1)
	v_max_i32_e32 v14, v8, v12
	v_min_i32_e32 v8, v8, v12
	s_xor_b64 s[18:19], s[10:11], s[16:17]
	v_cndmask_b32_e64 v8, v8, v14, s[18:19]
	ds_bpermute_b32 v12, v5, v11
	s_waitcnt lgkmcnt(1)
	v_max_i32_e32 v14, v10, v15
	v_min_i32_e32 v10, v10, v15
	v_cndmask_b32_e64 v10, v10, v14, s[18:19]
	ds_bpermute_b32 v14, v5, v9
	s_waitcnt lgkmcnt(1)
	v_max_i32_e32 v15, v11, v12
	v_min_i32_e32 v11, v11, v12
	ds_bpermute_b32 v12, v4, v8
	v_cndmask_b32_e64 v11, v11, v15, s[18:19]
	s_waitcnt lgkmcnt(1)
	v_max_i32_e32 v15, v9, v14
	v_min_i32_e32 v9, v9, v14
	v_cndmask_b32_e64 v9, v9, v15, s[18:19]
	ds_bpermute_b32 v15, v4, v10
	s_waitcnt lgkmcnt(1)
	v_max_i32_e32 v14, v8, v12
	v_min_i32_e32 v8, v8, v12
	s_xor_b64 s[18:19], s[8:9], s[16:17]
	v_cndmask_b32_e64 v8, v8, v14, s[18:19]
	ds_bpermute_b32 v12, v4, v11
	s_waitcnt lgkmcnt(1)
	v_max_i32_e32 v14, v10, v15
	v_min_i32_e32 v10, v10, v15
	v_cndmask_b32_e64 v10, v10, v14, s[18:19]
	ds_bpermute_b32 v14, v4, v9
	s_waitcnt lgkmcnt(1)
	v_max_i32_e32 v15, v11, v12
	v_min_i32_e32 v11, v11, v12
	ds_bpermute_b32 v12, v3, v8
	v_cndmask_b32_e64 v11, v11, v15, s[18:19]
	s_waitcnt lgkmcnt(1)
	v_max_i32_e32 v15, v9, v14
	v_min_i32_e32 v9, v9, v14
	v_cndmask_b32_e64 v9, v9, v15, s[18:19]
	ds_bpermute_b32 v15, v3, v10
	s_waitcnt lgkmcnt(1)
	v_max_i32_e32 v14, v8, v12
	v_min_i32_e32 v8, v8, v12
	s_xor_b64 s[18:19], s[6:7], s[16:17]
	v_cndmask_b32_e64 v8, v8, v14, s[18:19]
	ds_bpermute_b32 v12, v3, v11
	s_waitcnt lgkmcnt(1)
	v_max_i32_e32 v14, v10, v15
	v_min_i32_e32 v10, v10, v15
	v_cndmask_b32_e64 v10, v10, v14, s[18:19]
	ds_bpermute_b32 v14, v3, v9
	s_waitcnt lgkmcnt(1)
	v_max_i32_e32 v15, v11, v12
	v_min_i32_e32 v11, v11, v12
	ds_bpermute_b32 v12, v2, v8
	v_cndmask_b32_e64 v11, v11, v15, s[18:19]
	s_waitcnt lgkmcnt(1)
	v_max_i32_e32 v15, v9, v14
	v_min_i32_e32 v9, v9, v14
	v_cndmask_b32_e64 v9, v9, v15, s[18:19]
	ds_bpermute_b32 v15, v2, v10
	s_waitcnt lgkmcnt(1)
	v_max_i32_e32 v14, v8, v12
	v_min_i32_e32 v8, v8, v12
	s_xor_b64 s[16:17], vcc, s[16:17]
	ds_bpermute_b32 v12, v2, v11
	v_cndmask_b32_e64 v8, v8, v14, s[16:17]
	s_waitcnt lgkmcnt(1)
	v_max_i32_e32 v14, v10, v15
	v_min_i32_e32 v10, v10, v15
	ds_bpermute_b32 v15, v2, v9
	v_cndmask_b32_e64 v10, v10, v14, s[16:17]
	s_waitcnt lgkmcnt(1)
	v_max_i32_e32 v14, v11, v12
	v_min_i32_e32 v11, v11, v12
	v_cndmask_b32_e64 v11, v11, v14, s[16:17]
	s_waitcnt lgkmcnt(0)
	v_max_i32_e32 v12, v9, v15
	v_min_i32_e32 v9, v9, v15
	v_cndmask_b32_e64 v9, v9, v12, s[16:17]
	v_max_i32_e32 v12, v8, v11
	v_min_i32_e32 v8, v8, v11
	v_cmp_eq_u32_e64 s[16:17], 0, v13
	v_lshlrev_b32_e32 v208, 11, v82
	v_mov_b32_e32 v209, v197
	v_cndmask_b32_e64 v11, v8, v12, s[16:17]
	v_cndmask_b32_e64 v8, v12, v8, s[16:17]
	v_max_i32_e32 v12, v10, v9
	v_min_i32_e32 v9, v10, v9
	v_cndmask_b32_e64 v10, v9, v12, s[16:17]
	v_cndmask_b32_e64 v9, v12, v9, s[16:17]
	v_max_i32_e32 v13, v11, v10
	v_min_i32_e32 v10, v11, v10
	v_cndmask_b32_e64 v12, v10, v13, s[16:17]
	v_cndmask_b32_e64 v13, v13, v10, s[16:17]
	v_max_i32_e32 v10, v8, v9
	v_min_i32_e32 v8, v8, v9
	v_cndmask_b32_e64 v14, v8, v10, s[16:17]
	v_cndmask_b32_e64 v15, v10, v8, s[16:17]
	ds_write_b128 v1, v[12:15]
	v_xor_b32_e32 v8, 0x100, v252
	s_waitcnt lgkmcnt(0)
	s_barrier
	v_lshl_add_u32 v8, v8, 2, s30
	ds_read_b32 v16, v8
	v_and_b32_e32 v9, 0x80, v0
	v_cmp_ne_u32_e64 s[18:19], 0, v9
	v_xor_b32_e32 v9, 0x101, v252
	v_lshl_add_u32 v9, v9, 2, s30
	v_xor_b32_e32 v10, 0x102, v252
	v_xor_b32_e32 v11, 0x103, v252
	v_lshl_add_u32 v10, v10, 2, s30
	v_lshl_add_u32 v11, v11, 2, s30
	ds_read_b32 v18, v9
	ds_read_b32 v19, v10
	ds_read_b32 v20, v11
	s_waitcnt lgkmcnt(3)
	v_max_i32_e32 v21, v12, v16
	v_min_i32_e32 v12, v12, v16
	s_xor_b64 s[20:21], s[16:17], s[18:19]
	v_cndmask_b32_e64 v12, v12, v21, s[20:21]
	s_waitcnt lgkmcnt(2)
	v_max_i32_e32 v16, v13, v18
	v_min_i32_e32 v13, v13, v18
	v_cndmask_b32_e64 v13, v13, v16, s[20:21]
	ds_bpermute_b32 v18, v7, v12
	s_waitcnt lgkmcnt(2)
	v_max_i32_e32 v16, v14, v19
	v_min_i32_e32 v14, v14, v19
	ds_bpermute_b32 v19, v7, v13
	v_cndmask_b32_e64 v14, v14, v16, s[20:21]
	s_waitcnt lgkmcnt(2)
	v_max_i32_e32 v16, v15, v20
	v_min_i32_e32 v15, v15, v20
	v_cndmask_b32_e64 v15, v15, v16, s[20:21]
	s_waitcnt lgkmcnt(1)
	v_max_i32_e32 v16, v12, v18
	v_min_i32_e32 v12, v12, v18
	s_xor_b64 s[20:21], s[14:15], s[18:19]
	v_cndmask_b32_e64 v12, v12, v16, s[20:21]
	ds_bpermute_b32 v16, v7, v14
	s_waitcnt lgkmcnt(1)
	v_max_i32_e32 v18, v13, v19
	v_min_i32_e32 v13, v13, v19
	v_cndmask_b32_e64 v13, v13, v18, s[20:21]
	ds_bpermute_b32 v18, v7, v15
	s_waitcnt lgkmcnt(1)
	v_max_i32_e32 v19, v14, v16
	v_min_i32_e32 v14, v14, v16
	ds_bpermute_b32 v16, v6, v12
	v_cndmask_b32_e64 v14, v14, v19, s[20:21]
	s_waitcnt lgkmcnt(1)
	v_max_i32_e32 v19, v15, v18
	v_min_i32_e32 v15, v15, v18
	v_cndmask_b32_e64 v15, v15, v19, s[20:21]
	ds_bpermute_b32 v19, v6, v13
	s_waitcnt lgkmcnt(1)
	v_max_i32_e32 v18, v12, v16
	v_min_i32_e32 v12, v12, v16
	s_xor_b64 s[20:21], s[12:13], s[18:19]
	v_cndmask_b32_e64 v12, v12, v18, s[20:21]
	ds_bpermute_b32 v16, v6, v14
	s_waitcnt lgkmcnt(1)
	v_max_i32_e32 v18, v13, v19
	v_min_i32_e32 v13, v13, v19
	v_cndmask_b32_e64 v13, v13, v18, s[20:21]
	ds_bpermute_b32 v18, v6, v15
	s_waitcnt lgkmcnt(1)
	v_max_i32_e32 v19, v14, v16
	v_min_i32_e32 v14, v14, v16
	ds_bpermute_b32 v16, v5, v12
	v_cndmask_b32_e64 v14, v14, v19, s[20:21]
	s_waitcnt lgkmcnt(1)
	v_max_i32_e32 v19, v15, v18
	v_min_i32_e32 v15, v15, v18
	v_cndmask_b32_e64 v15, v15, v19, s[20:21]
	ds_bpermute_b32 v19, v5, v13
	s_waitcnt lgkmcnt(1)
	v_max_i32_e32 v18, v12, v16
	v_min_i32_e32 v12, v12, v16
	s_xor_b64 s[20:21], s[10:11], s[18:19]
	v_cndmask_b32_e64 v12, v12, v18, s[20:21]
	ds_bpermute_b32 v16, v5, v14
	s_waitcnt lgkmcnt(1)
	v_max_i32_e32 v18, v13, v19
	v_min_i32_e32 v13, v13, v19
	v_cndmask_b32_e64 v13, v13, v18, s[20:21]
	ds_bpermute_b32 v18, v5, v15
	s_waitcnt lgkmcnt(1)
	v_max_i32_e32 v19, v14, v16
	v_min_i32_e32 v14, v14, v16
	ds_bpermute_b32 v16, v4, v12
	v_cndmask_b32_e64 v14, v14, v19, s[20:21]
	s_waitcnt lgkmcnt(1)
	v_max_i32_e32 v19, v15, v18
	v_min_i32_e32 v15, v15, v18
	v_cndmask_b32_e64 v15, v15, v19, s[20:21]
	ds_bpermute_b32 v19, v4, v13
	s_waitcnt lgkmcnt(1)
	v_max_i32_e32 v18, v12, v16
	v_min_i32_e32 v12, v12, v16
	s_xor_b64 s[20:21], s[8:9], s[18:19]
	v_cndmask_b32_e64 v12, v12, v18, s[20:21]
	ds_bpermute_b32 v16, v4, v14
	s_waitcnt lgkmcnt(1)
	v_max_i32_e32 v18, v13, v19
	v_min_i32_e32 v13, v13, v19
	v_cndmask_b32_e64 v13, v13, v18, s[20:21]
	ds_bpermute_b32 v18, v4, v15
	s_waitcnt lgkmcnt(1)
	v_max_i32_e32 v19, v14, v16
	v_min_i32_e32 v14, v14, v16
	ds_bpermute_b32 v16, v3, v12
	v_cndmask_b32_e64 v14, v14, v19, s[20:21]
	s_waitcnt lgkmcnt(1)
	v_max_i32_e32 v19, v15, v18
	v_min_i32_e32 v15, v15, v18
	v_cndmask_b32_e64 v15, v15, v19, s[20:21]
	ds_bpermute_b32 v19, v3, v13
	s_waitcnt lgkmcnt(1)
	v_max_i32_e32 v18, v12, v16
	v_min_i32_e32 v12, v12, v16
	s_xor_b64 s[20:21], s[6:7], s[18:19]
	v_cndmask_b32_e64 v12, v12, v18, s[20:21]
	ds_bpermute_b32 v16, v3, v14
	s_waitcnt lgkmcnt(1)
	v_max_i32_e32 v18, v13, v19
	v_min_i32_e32 v13, v13, v19
	v_cndmask_b32_e64 v13, v13, v18, s[20:21]
	ds_bpermute_b32 v18, v3, v15
	s_waitcnt lgkmcnt(1)
	v_max_i32_e32 v19, v14, v16
	v_min_i32_e32 v14, v14, v16
	ds_bpermute_b32 v16, v2, v12
	v_cndmask_b32_e64 v14, v14, v19, s[20:21]
	s_waitcnt lgkmcnt(1)
	v_max_i32_e32 v19, v15, v18
	v_min_i32_e32 v15, v15, v18
	v_cndmask_b32_e64 v15, v15, v19, s[20:21]
	ds_bpermute_b32 v19, v2, v13
	s_waitcnt lgkmcnt(1)
	v_max_i32_e32 v18, v12, v16
	v_min_i32_e32 v12, v12, v16
	s_xor_b64 s[18:19], vcc, s[18:19]
	ds_bpermute_b32 v16, v2, v14
	v_cndmask_b32_e64 v12, v12, v18, s[18:19]
	s_waitcnt lgkmcnt(1)
	v_max_i32_e32 v18, v13, v19
	v_min_i32_e32 v13, v13, v19
	ds_bpermute_b32 v19, v2, v15
	v_cndmask_b32_e64 v13, v13, v18, s[18:19]
	s_waitcnt lgkmcnt(1)
	v_max_i32_e32 v18, v14, v16
	v_min_i32_e32 v14, v14, v16
	v_cndmask_b32_e64 v14, v14, v18, s[18:19]
	s_waitcnt lgkmcnt(0)
	v_max_i32_e32 v16, v15, v19
	v_min_i32_e32 v15, v15, v19
	v_cndmask_b32_e64 v15, v15, v16, s[18:19]
	v_max_i32_e32 v16, v12, v14
	v_min_i32_e32 v12, v12, v14
	v_cmp_eq_u32_e64 s[18:19], 0, v17
	s_waitcnt lgkmcnt(0)
	s_barrier
	v_and_b32_e32 v18, 0x100, v0
	v_cmp_ne_u32_e64 s[20:21], 0, v18
	v_cndmask_b32_e64 v14, v12, v16, s[18:19]
	v_cndmask_b32_e64 v16, v16, v12, s[18:19]
	v_max_i32_e32 v12, v13, v15
	v_min_i32_e32 v13, v13, v15
	v_cndmask_b32_e64 v15, v13, v12, s[18:19]
	v_cndmask_b32_e64 v17, v12, v13, s[18:19]
	v_max_i32_e32 v13, v14, v15
	v_min_i32_e32 v14, v14, v15
	v_max_i32_e32 v15, v16, v17
	v_min_i32_e32 v16, v16, v17
	v_cndmask_b32_e64 v12, v14, v13, s[18:19]
	v_cndmask_b32_e64 v13, v13, v14, s[18:19]
	v_cndmask_b32_e64 v14, v16, v15, s[18:19]
	v_cndmask_b32_e64 v15, v15, v16, s[18:19]
	ds_write_b128 v1, v[12:15]
	v_xor_b32_e32 v16, 0x200, v252
	s_waitcnt lgkmcnt(0)
	s_barrier
	v_lshl_add_u32 v16, v16, 2, s30
	ds_read_b32 v17, v16
	v_xor_b32_e32 v18, 0x201, v252
	v_lshl_add_u32 v18, v18, 2, s30
	v_xor_b32_e32 v19, 0x202, v252
	v_xor_b32_e32 v20, 0x203, v252
	v_lshl_add_u32 v19, v19, 2, s30
	v_lshl_add_u32 v20, v20, 2, s30
	ds_read_b32 v21, v18
	ds_read_b32 v22, v19
	ds_read_b32 v23, v20
	s_waitcnt lgkmcnt(3)
	v_max_i32_e32 v24, v12, v17
	v_min_i32_e32 v12, v12, v17
	s_xor_b64 s[22:23], s[18:19], s[20:21]
	s_waitcnt lgkmcnt(2)
	v_max_i32_e32 v17, v13, v21
	v_min_i32_e32 v13, v13, v21
	v_cndmask_b32_e64 v13, v13, v17, s[22:23]
	s_waitcnt lgkmcnt(1)
	v_max_i32_e32 v17, v14, v22
	v_min_i32_e32 v14, v14, v22
	v_cndmask_b32_e64 v14, v14, v17, s[22:23]
	s_waitcnt lgkmcnt(0)
	v_max_i32_e32 v17, v15, v23
	v_min_i32_e32 v15, v15, v23
	v_cndmask_b32_e64 v12, v12, v24, s[22:23]
	v_cndmask_b32_e64 v15, v15, v17, s[22:23]
	s_waitcnt lgkmcnt(0)
	s_barrier
	ds_write_b128 v1, v[12:15]
	s_waitcnt lgkmcnt(0)
	s_barrier
	ds_read_b32 v17, v8
	ds_read_b32 v22, v9
	ds_read_b32 v23, v10
	ds_read_b32 v24, v11
	s_xor_b64 s[22:23], s[16:17], s[20:21]
	v_and_b32_e32 v21, 0x100, v0
	s_waitcnt lgkmcnt(0)
	s_barrier
	s_waitcnt lgkmcnt(3)
	v_max_i32_e32 v25, v12, v17
	v_min_i32_e32 v12, v12, v17
	v_cndmask_b32_e64 v12, v12, v25, s[22:23]
	s_waitcnt lgkmcnt(2)
	v_max_i32_e32 v17, v13, v22
	v_min_i32_e32 v13, v13, v22
	v_cndmask_b32_e64 v13, v13, v17, s[22:23]
	ds_bpermute_b32 v22, v7, v12
	s_waitcnt lgkmcnt(2)
	v_max_i32_e32 v17, v14, v23
	v_min_i32_e32 v14, v14, v23
	ds_bpermute_b32 v23, v7, v13
	v_cndmask_b32_e64 v14, v14, v17, s[22:23]
	s_waitcnt lgkmcnt(2)
	v_max_i32_e32 v17, v15, v24
	v_min_i32_e32 v15, v15, v24
	v_cndmask_b32_e64 v15, v15, v17, s[22:23]
	s_waitcnt lgkmcnt(1)
	v_max_i32_e32 v17, v12, v22
	v_min_i32_e32 v12, v12, v22
	s_xor_b64 s[22:23], s[14:15], s[20:21]
	v_cndmask_b32_e64 v12, v12, v17, s[22:23]
	ds_bpermute_b32 v17, v7, v14
	s_waitcnt lgkmcnt(1)
	v_max_i32_e32 v22, v13, v23
	v_min_i32_e32 v13, v13, v23
	v_cndmask_b32_e64 v13, v13, v22, s[22:23]
	ds_bpermute_b32 v22, v7, v15
	s_waitcnt lgkmcnt(1)
	v_max_i32_e32 v23, v14, v17
	v_min_i32_e32 v14, v14, v17
	ds_bpermute_b32 v17, v6, v12
	v_cndmask_b32_e64 v14, v14, v23, s[22:23]
	s_waitcnt lgkmcnt(1)
	v_max_i32_e32 v23, v15, v22
	v_min_i32_e32 v15, v15, v22
	v_cndmask_b32_e64 v15, v15, v23, s[22:23]
	ds_bpermute_b32 v23, v6, v13
	s_waitcnt lgkmcnt(1)
	v_max_i32_e32 v22, v12, v17
	v_min_i32_e32 v12, v12, v17
	s_xor_b64 s[22:23], s[12:13], s[20:21]
	v_cndmask_b32_e64 v12, v12, v22, s[22:23]
	ds_bpermute_b32 v17, v6, v14
	s_waitcnt lgkmcnt(1)
	v_max_i32_e32 v22, v13, v23
	v_min_i32_e32 v13, v13, v23
	v_cndmask_b32_e64 v13, v13, v22, s[22:23]
	ds_bpermute_b32 v22, v6, v15
	s_waitcnt lgkmcnt(1)
	v_max_i32_e32 v23, v14, v17
	v_min_i32_e32 v14, v14, v17
	ds_bpermute_b32 v17, v5, v12
	v_cndmask_b32_e64 v14, v14, v23, s[22:23]
	s_waitcnt lgkmcnt(1)
	v_max_i32_e32 v23, v15, v22
	v_min_i32_e32 v15, v15, v22
	v_cndmask_b32_e64 v15, v15, v23, s[22:23]
	ds_bpermute_b32 v23, v5, v13
	s_waitcnt lgkmcnt(1)
	v_max_i32_e32 v22, v12, v17
	v_min_i32_e32 v12, v12, v17
	s_xor_b64 s[22:23], s[10:11], s[20:21]
	v_cndmask_b32_e64 v12, v12, v22, s[22:23]
	ds_bpermute_b32 v17, v5, v14
	s_waitcnt lgkmcnt(1)
	v_max_i32_e32 v22, v13, v23
	v_min_i32_e32 v13, v13, v23
	v_cndmask_b32_e64 v13, v13, v22, s[22:23]
	ds_bpermute_b32 v22, v5, v15
	s_waitcnt lgkmcnt(1)
	v_max_i32_e32 v23, v14, v17
	v_min_i32_e32 v14, v14, v17
	ds_bpermute_b32 v17, v4, v12
	v_cndmask_b32_e64 v14, v14, v23, s[22:23]
	s_waitcnt lgkmcnt(1)
	v_max_i32_e32 v23, v15, v22
	v_min_i32_e32 v15, v15, v22
	v_cndmask_b32_e64 v15, v15, v23, s[22:23]
	ds_bpermute_b32 v23, v4, v13
	s_waitcnt lgkmcnt(1)
	v_max_i32_e32 v22, v12, v17
	v_min_i32_e32 v12, v12, v17
	s_xor_b64 s[22:23], s[8:9], s[20:21]
	v_cndmask_b32_e64 v12, v12, v22, s[22:23]
	ds_bpermute_b32 v17, v4, v14
	s_waitcnt lgkmcnt(1)
	v_max_i32_e32 v22, v13, v23
	v_min_i32_e32 v13, v13, v23
	v_cndmask_b32_e64 v13, v13, v22, s[22:23]
	ds_bpermute_b32 v22, v4, v15
	s_waitcnt lgkmcnt(1)
	v_max_i32_e32 v23, v14, v17
	v_min_i32_e32 v14, v14, v17
	ds_bpermute_b32 v17, v3, v12
	v_cndmask_b32_e64 v14, v14, v23, s[22:23]
	s_waitcnt lgkmcnt(1)
	v_max_i32_e32 v23, v15, v22
	v_min_i32_e32 v15, v15, v22
	v_cndmask_b32_e64 v15, v15, v23, s[22:23]
	ds_bpermute_b32 v23, v3, v13
	s_waitcnt lgkmcnt(1)
	v_max_i32_e32 v22, v12, v17
	v_min_i32_e32 v12, v12, v17
	s_xor_b64 s[22:23], s[6:7], s[20:21]
	v_cndmask_b32_e64 v12, v12, v22, s[22:23]
	ds_bpermute_b32 v17, v3, v14
	s_waitcnt lgkmcnt(1)
	v_max_i32_e32 v22, v13, v23
	v_min_i32_e32 v13, v13, v23
	v_cndmask_b32_e64 v13, v13, v22, s[22:23]
	ds_bpermute_b32 v22, v3, v15
	s_waitcnt lgkmcnt(1)
	v_max_i32_e32 v23, v14, v17
	v_min_i32_e32 v14, v14, v17
	ds_bpermute_b32 v17, v2, v12
	v_cndmask_b32_e64 v14, v14, v23, s[22:23]
	s_waitcnt lgkmcnt(1)
	v_max_i32_e32 v23, v15, v22
	v_min_i32_e32 v15, v15, v22
	v_cndmask_b32_e64 v15, v15, v23, s[22:23]
	ds_bpermute_b32 v23, v2, v13
	s_waitcnt lgkmcnt(1)
	v_max_i32_e32 v22, v12, v17
	v_min_i32_e32 v12, v12, v17
	s_xor_b64 s[20:21], vcc, s[20:21]
	ds_bpermute_b32 v17, v2, v14
	v_cndmask_b32_e64 v12, v12, v22, s[20:21]
	s_waitcnt lgkmcnt(1)
	v_max_i32_e32 v22, v13, v23
	v_min_i32_e32 v13, v13, v23
	ds_bpermute_b32 v23, v2, v15
	v_cndmask_b32_e64 v13, v13, v22, s[20:21]
	s_waitcnt lgkmcnt(1)
	v_max_i32_e32 v22, v14, v17
	v_min_i32_e32 v14, v14, v17
	v_cndmask_b32_e64 v14, v14, v22, s[20:21]
	s_waitcnt lgkmcnt(0)
	v_max_i32_e32 v17, v15, v23
	v_min_i32_e32 v15, v15, v23
	v_cndmask_b32_e64 v15, v15, v17, s[20:21]
	v_max_i32_e32 v17, v12, v14
	v_min_i32_e32 v12, v12, v14
	v_cmp_eq_u32_e64 s[22:23], 0, v21
	v_xor_b32_e32 v22, 0x402, v252
	v_xor_b32_e32 v23, 0x403, v252
	v_cndmask_b32_e64 v14, v12, v17, s[22:23]
	v_cndmask_b32_e64 v17, v17, v12, s[22:23]
	v_max_i32_e32 v12, v13, v15
	v_min_i32_e32 v13, v13, v15
	v_cndmask_b32_e64 v15, v13, v12, s[22:23]
	v_cndmask_b32_e64 v21, v12, v13, s[22:23]
	v_max_i32_e32 v13, v14, v15
	v_min_i32_e32 v14, v14, v15
	v_max_i32_e32 v15, v17, v21
	v_min_i32_e32 v17, v17, v21
	v_cndmask_b32_e64 v12, v14, v13, s[22:23]
	v_cndmask_b32_e64 v13, v13, v14, s[22:23]
	v_cndmask_b32_e64 v14, v17, v15, s[22:23]
	v_cndmask_b32_e64 v15, v15, v17, s[22:23]
	ds_write_b128 v1, v[12:15]
	v_xor_b32_e32 v17, 0x400, v252
	s_waitcnt lgkmcnt(0)
	s_barrier
	v_lshl_add_u32 v17, v17, 2, s30
	ds_read_b32 v17, v17
	v_xor_b32_e32 v21, 0x401, v252
	v_lshl_add_u32 v21, v21, 2, s30
	v_lshl_add_u32 v22, v22, 2, s30
	v_lshl_add_u32 v23, v23, 2, s30
	ds_read_b32 v21, v21
	ds_read_b32 v22, v22
	ds_read_b32 v23, v23
	s_movk_i32 s20, 0x1ff
	v_cmp_lt_u32_e64 s[20:21], s20, v0
	s_waitcnt lgkmcnt(3)
	v_max_i32_e32 v24, v12, v17
	v_min_i32_e32 v12, v12, v17
	s_xor_b64 s[22:23], s[22:23], s[20:21]
	s_waitcnt lgkmcnt(2)
	v_max_i32_e32 v17, v13, v21
	v_min_i32_e32 v13, v13, v21
	v_cndmask_b32_e64 v13, v13, v17, s[22:23]
	s_waitcnt lgkmcnt(1)
	v_max_i32_e32 v17, v14, v22
	v_min_i32_e32 v14, v14, v22
	v_cndmask_b32_e64 v14, v14, v17, s[22:23]
	s_waitcnt lgkmcnt(0)
	v_max_i32_e32 v17, v15, v23
	v_min_i32_e32 v15, v15, v23
	v_cndmask_b32_e64 v12, v12, v24, s[22:23]
	v_cndmask_b32_e64 v15, v15, v17, s[22:23]
	s_waitcnt lgkmcnt(0)
	s_barrier
	ds_write_b128 v1, v[12:15]
	s_waitcnt lgkmcnt(0)
	s_barrier
	ds_read_b32 v16, v16
	ds_read_b32 v17, v18
	ds_read_b32 v18, v19
	ds_read_b32 v19, v20
	s_xor_b64 s[18:19], s[18:19], s[20:21]
	s_waitcnt lgkmcnt(0)
	s_barrier
	s_xor_b64 s[16:17], s[16:17], s[20:21]
	s_waitcnt lgkmcnt(3)
	v_max_i32_e32 v20, v12, v16
	v_min_i32_e32 v12, v12, v16
	s_waitcnt lgkmcnt(2)
	v_max_i32_e32 v16, v13, v17
	v_min_i32_e32 v13, v13, v17
	v_cndmask_b32_e64 v13, v13, v16, s[18:19]
	s_waitcnt lgkmcnt(1)
	v_max_i32_e32 v16, v14, v18
	v_min_i32_e32 v14, v14, v18
	v_cndmask_b32_e64 v14, v14, v16, s[18:19]
	s_waitcnt lgkmcnt(0)
	v_max_i32_e32 v16, v15, v19
	v_min_i32_e32 v15, v15, v19
	v_cndmask_b32_e64 v12, v12, v20, s[18:19]
	v_cndmask_b32_e64 v15, v15, v16, s[18:19]
	ds_write_b128 v1, v[12:15]
	s_waitcnt lgkmcnt(0)
	s_barrier
	ds_read_b32 v8, v8
	ds_read_b32 v9, v9
	ds_read_b32 v10, v10
	ds_read_b32 v11, v11
	s_xor_b64 s[14:15], s[14:15], s[20:21]
	s_xor_b64 s[12:13], s[12:13], s[20:21]
	s_xor_b64 s[10:11], s[10:11], s[20:21]
	s_waitcnt lgkmcnt(3)
	v_max_i32_e32 v16, v12, v8
	v_min_i32_e32 v8, v12, v8
	v_cndmask_b32_e64 v8, v8, v16, s[16:17]
	s_waitcnt lgkmcnt(2)
	v_max_i32_e32 v12, v13, v9
	v_min_i32_e32 v9, v13, v9
	ds_bpermute_b32 v13, v7, v8
	v_cndmask_b32_e64 v9, v9, v12, s[16:17]
	s_waitcnt lgkmcnt(2)
	v_max_i32_e32 v12, v14, v10
	v_min_i32_e32 v10, v14, v10
	v_cndmask_b32_e64 v10, v10, v12, s[16:17]
	s_waitcnt lgkmcnt(1)
	v_max_i32_e32 v12, v15, v11
	v_min_i32_e32 v11, v15, v11
	v_cndmask_b32_e64 v11, v11, v12, s[16:17]
	s_waitcnt lgkmcnt(0)
	v_max_i32_e32 v12, v8, v13
	ds_bpermute_b32 v14, v7, v9
	v_min_i32_e32 v8, v8, v13
	v_cndmask_b32_e64 v8, v8, v12, s[14:15]
	ds_bpermute_b32 v12, v7, v10
	ds_bpermute_b32 v7, v7, v11
	s_waitcnt lgkmcnt(2)
	v_max_i32_e32 v13, v9, v14
	v_min_i32_e32 v9, v9, v14
	v_cndmask_b32_e64 v9, v9, v13, s[14:15]
	s_waitcnt lgkmcnt(1)
	v_max_i32_e32 v13, v10, v12
	v_min_i32_e32 v10, v10, v12
	ds_bpermute_b32 v12, v6, v8
	v_cndmask_b32_e64 v10, v10, v13, s[14:15]
	s_waitcnt lgkmcnt(1)
	v_max_i32_e32 v13, v11, v7
	v_min_i32_e32 v7, v11, v7
	v_cndmask_b32_e64 v7, v7, v13, s[14:15]
	s_waitcnt lgkmcnt(0)
	v_max_i32_e32 v11, v8, v12
	ds_bpermute_b32 v13, v6, v9
	v_min_i32_e32 v8, v8, v12
	v_cndmask_b32_e64 v8, v8, v11, s[12:13]
	ds_bpermute_b32 v11, v6, v10
	ds_bpermute_b32 v6, v6, v7
	s_waitcnt lgkmcnt(2)
	v_max_i32_e32 v12, v9, v13
	v_min_i32_e32 v9, v9, v13
	v_cndmask_b32_e64 v9, v9, v12, s[12:13]
	s_waitcnt lgkmcnt(1)
	v_max_i32_e32 v12, v10, v11
	v_min_i32_e32 v10, v10, v11
	ds_bpermute_b32 v11, v5, v8
	v_cndmask_b32_e64 v10, v10, v12, s[12:13]
	s_waitcnt lgkmcnt(1)
	v_max_i32_e32 v12, v7, v6
	v_min_i32_e32 v6, v7, v6
	v_cndmask_b32_e64 v6, v6, v12, s[12:13]
	s_waitcnt lgkmcnt(0)
	v_max_i32_e32 v7, v8, v11
	ds_bpermute_b32 v12, v5, v9
	v_min_i32_e32 v8, v8, v11
	v_cndmask_b32_e64 v7, v8, v7, s[10:11]
	ds_bpermute_b32 v8, v5, v10
	ds_bpermute_b32 v5, v5, v6
	s_waitcnt lgkmcnt(2)
	v_max_i32_e32 v11, v9, v12
	v_min_i32_e32 v9, v9, v12
	v_cndmask_b32_e64 v9, v9, v11, s[10:11]
	s_waitcnt lgkmcnt(1)
	v_max_i32_e32 v11, v10, v8
	v_min_i32_e32 v8, v10, v8
	ds_bpermute_b32 v10, v4, v7
	v_cndmask_b32_e64 v8, v8, v11, s[10:11]
	s_waitcnt lgkmcnt(1)
	v_max_i32_e32 v11, v6, v5
	v_min_i32_e32 v5, v6, v5
	v_cndmask_b32_e64 v5, v5, v11, s[10:11]
	s_waitcnt lgkmcnt(0)
	v_max_i32_e32 v6, v7, v10
	ds_bpermute_b32 v11, v4, v9
	v_min_i32_e32 v7, v7, v10
	s_xor_b64 s[8:9], s[8:9], s[20:21]
	v_cndmask_b32_e64 v6, v7, v6, s[8:9]
	ds_bpermute_b32 v7, v4, v8
	s_waitcnt lgkmcnt(1)
	v_max_i32_e32 v10, v9, v11
	v_min_i32_e32 v9, v9, v11
	ds_bpermute_b32 v4, v4, v5
	v_cndmask_b32_e64 v9, v9, v10, s[8:9]
	s_waitcnt lgkmcnt(1)
	v_max_i32_e32 v10, v8, v7
	v_min_i32_e32 v7, v8, v7
	ds_bpermute_b32 v8, v3, v6
	v_cndmask_b32_e64 v7, v7, v10, s[8:9]
	s_waitcnt lgkmcnt(1)
	v_max_i32_e32 v10, v5, v4
	v_min_i32_e32 v4, v5, v4
	v_cndmask_b32_e64 v4, v4, v10, s[8:9]
	s_waitcnt lgkmcnt(0)
	v_max_i32_e32 v5, v6, v8
	ds_bpermute_b32 v10, v3, v9
	v_min_i32_e32 v6, v6, v8
	s_xor_b64 s[6:7], s[6:7], s[20:21]
	v_cndmask_b32_e64 v5, v6, v5, s[6:7]
	ds_bpermute_b32 v6, v3, v7
	s_waitcnt lgkmcnt(1)
	v_max_i32_e32 v8, v9, v10
	v_min_i32_e32 v9, v9, v10
	ds_bpermute_b32 v3, v3, v4
	v_cndmask_b32_e64 v8, v9, v8, s[6:7]
	s_waitcnt lgkmcnt(1)
	v_max_i32_e32 v9, v7, v6
	v_min_i32_e32 v6, v7, v6
	ds_bpermute_b32 v7, v2, v5
	v_cndmask_b32_e64 v6, v6, v9, s[6:7]
	s_waitcnt lgkmcnt(1)
	v_max_i32_e32 v9, v4, v3
	v_min_i32_e32 v3, v4, v3
	v_cndmask_b32_e64 v3, v3, v9, s[6:7]
	s_waitcnt lgkmcnt(0)
	v_max_i32_e32 v4, v5, v7
	ds_bpermute_b32 v9, v2, v8
	v_min_i32_e32 v5, v5, v7
	s_xor_b64 vcc, vcc, s[20:21]
	v_cndmask_b32_e32 v4, v5, v4, vcc
	ds_bpermute_b32 v5, v2, v6
	ds_bpermute_b32 v2, v2, v3
	s_waitcnt lgkmcnt(2)
	v_max_i32_e32 v7, v8, v9
	v_min_i32_e32 v8, v8, v9
	v_cndmask_b32_e32 v7, v8, v7, vcc
	s_waitcnt lgkmcnt(1)
	v_max_i32_e32 v8, v6, v5
	v_min_i32_e32 v5, v6, v5
	s_movk_i32 s18, 0x200
	v_cndmask_b32_e32 v5, v5, v8, vcc
	s_waitcnt lgkmcnt(0)
	v_max_i32_e32 v6, v3, v2
	v_min_i32_e32 v2, v3, v2
	v_cndmask_b32_e32 v2, v2, v6, vcc
	v_max_i32_e32 v3, v4, v5
	v_min_i32_e32 v4, v4, v5
	v_cmp_gt_u32_e32 vcc, s18, v0
	s_add_i32 s8, 0, 0x20100
	s_cmp_lg_u32 0, -1
	v_cndmask_b32_e32 v5, v4, v3, vcc
	v_cndmask_b32_e32 v4, v3, v4, vcc
	v_max_i32_e32 v3, v7, v2
	v_min_i32_e32 v2, v7, v2
	v_cndmask_b32_e32 v6, v2, v3, vcc
	v_cndmask_b32_e32 v7, v3, v2, vcc
	v_max_i32_e32 v3, v5, v6
	v_min_i32_e32 v5, v5, v6
	v_cndmask_b32_e32 v2, v5, v3, vcc
	v_cndmask_b32_e32 v3, v3, v5, vcc
	v_max_i32_e32 v5, v4, v7
	v_min_i32_e32 v6, v4, v7
	v_cndmask_b32_e32 v4, v6, v5, vcc
	v_cndmask_b32_e32 v5, v5, v6, vcc
	s_waitcnt lgkmcnt(0)
	s_barrier
	ds_write_b128 v1, v[2:5]
	v_lshl_add_u32 v230, v0, 2, s8
	v_lshrrev_b32_e32 v3, 5, v82
	s_cselect_b32 s8, 0, 0
	v_and_b32_e32 v1, 32, v193
	s_addk_i32 s8, 0x6000
	v_lshlrev_b32_e32 v231, 2, v3
	v_lshrrev_b32_e32 v4, 2, v0
	v_add_u32_e32 v5, s8, v1
	v_and_or_b32 v4, v4, 3, v231
	v_add_u32_e32 v9, 0, v1
	v_lshlrev_b32_e32 v1, 10, v205
	s_movk_i32 s22, 0x100
	v_and_b32_e32 v2, 24, v158
	v_lshlrev_b32_e32 v6, 6, v4
	v_lshlrev_b32_e32 v7, 10, v3
	v_lshl_or_b32 v4, v3, 3, v1
	s_add_i32 s8, 0, 0x15000
	v_lshlrev_b32_e32 v1, 4, v3
	v_lshlrev_b32_e32 v207, 9, v3
	v_lshrrev_b32_e32 v3, 3, v82
	v_cmp_gt_u32_e64 s[6:7], s22, v0
	v_add_u32_e32 v233, s8, v1
	v_add3_u32 v234, v5, v2, v6
	v_or_b32_e32 v5, 8, v3
	v_add_u32_e32 v236, s8, v250
	v_readlane_b32 s8, v253, 46
	v_lshlrev_b32_e32 v8, 4, v205
	v_lshlrev_b32_e32 v195, 7, v3
	v_lshlrev_b32_e32 v200, 10, v3
	v_lshlrev_b32_e32 v199, 7, v5
	v_lshlrev_b32_e32 v202, 10, v5
	v_or_b32_e32 v5, 16, v3
	v_or_b32_e32 v3, 24, v3
	v_readlane_b32 s9, v253, 47
	v_readlane_b32 s20, v253, 58
	v_readlane_b32 s21, v253, 59
	v_readlane_b32 s22, v253, 60
	v_readlane_b32 s23, v253, 61
	v_add3_u32 v232, 0, v7, v8
	v_add3_u32 v235, v9, v2, v6
	v_lshlrev_b32_e32 v203, 7, v3
	v_lshlrev_b32_e32 v206, 10, v3
	v_readlane_b32 s10, v253, 48
	v_readlane_b32 s11, v253, 49
	v_readlane_b32 s12, v253, 50
	v_readlane_b32 s13, v253, 51
	v_readlane_b32 s14, v253, 52
	v_readlane_b32 s15, v253, 53
	v_readlane_b32 s16, v253, 54
	v_readlane_b32 s17, v253, 55
	v_readlane_b32 s18, v253, 56
	v_readlane_b32 s19, v253, 57
	v_lshl_add_u64 v[6:7], s[22:23], 0, v[250:251]
	s_mov_b64 s[8:9], 0x1480000
	v_add_u32_e32 v3, 0, v1
	s_mov_b32 s20, 0xfffe0000
	v_and_b32_e32 v198, 56, v158
	v_lshlrev_b32_e32 v201, 7, v5
	v_lshlrev_b32_e32 v204, 10, v5
	v_lshl_add_u64 v[210:211], v[6:7], 0, s[8:9]
	v_add_u32_e32 v241, 0x15100, v3
	v_or_b32_e32 v237, 0x17b, v231
	s_mov_b64 s[10:11], 0x2000
	v_lshlrev_b32_e32 v212, 1, v2
	s_mov_b64 s[12:13], 0x20000
	v_lshlrev_b32_e32 v238, 1, v4
	s_mov_b64 s[14:15], 0x40000
	s_mov_b64 s[16:17], 0x60000
	s_mov_b64 s[18:19], 0xa0000
	s_mov_b32 s21, -1
	s_mov_b64 s[22:23], 0x80000
	s_movk_i32 s46, 0x1000
	v_mov_b32_e32 v239, 0x7f800000
	v_mov_b32_e32 v240, 0xff800000
	s_mov_b32 s47, 0
	s_cmp_lg_u32 s92, 0
	s_cbranch_scc1 .Lgw_end_9
	v_mov_b32_e32 v2, 0x22160
	ds_read_b32 v246, v2
	s_lshr_b32 s8, s99, 16
	s_add_u32 s8, s100, s8
	s_addc_u32 s9, s101, 0
	s_min_u32 s30, s98, 8
	v_mov_b32_e32 v2, 0
	v_mov_b32_e32 v247, 0
	s_waitcnt lgkmcnt(0)
	v_readfirstlane_b32 vcc_lo, v246
	s_mul_i32 s30, s30, vcc_lo
.Lgw_poll_9:
	global_load_dword v246, v2, s[8:9] sc1
	v_add_u32_e32 v247, 1, v247
	s_waitcnt vmcnt(0)
	v_cmp_le_u32_e32 vcc, s30, v246
	s_cbranch_vccnz .Lgw_end_9
	v_cmp_gt_u32_e32 vcc, 0x80000, v247
	s_sleep 1
	s_cbranch_vccnz .Lgw_poll_9
.Lgw_end_9:
	s_waitcnt lgkmcnt(0)
	s_barrier
	s_branch .LBB0_1689
